# best (Gt relayout + hand-scheduled P6 gate epilogue + nt gate loads) plus P2 post-K-loop drain vmcnt(0) counted down to vmcnt(8)
# speedup vs baseline: 1.0263x; 1.0263x over previous
; #define PG8_STAGE(bufoff, gbase, voff) do { _Pragma("unroll") for (int _i = 0; _i < 2; ++_i) \
;         __builtin_amdgcn_global_load_lds((const unsigned*)((const char*)(gbase) + (voff)[_i]), (PG8_LAS unsigned*)(lds + (bufoff) + ldsw + _i * 8192), 16, 0, 0); } while (0)
; #define PG8_LDA(dst, b, h) do { _Pragma("unroll") for (int m = 0; m < 4; ++m) _Pragma("unroll") for (int k = 0; k < 2; ++k) dst[m][k] = *(const PG8_LAS bf16x8*)(lds + PG8_SA(b, h) + aoff + m * 2048 + k * 1024); } while (0)
; #define PG8_LDB(dst, b, h) do { _Pragma("unroll") for (int n = 0; n < 2; ++n) _Pragma("unroll") for (int k = 0; k < 2; ++k) dst[n][k] = *(const PG8_LAS bf16x8*)(lds + PG8_SB(b, h) + boff + n * 2048 + k * 1024); } while (0)
; #define PG8_MMA(ai, bj, At, Bt) do { __builtin_amdgcn_s_setprio(1); _Pragma("unroll") for (int m = 0; m < 4; ++m) _Pragma("unroll") for (int n = 0; n < 2; ++n) _Pragma("unroll") for (int k = 0; k < 2; ++k) \
;         acc[ai][bj][m][n] = __builtin_amdgcn_mfma_f32_16x16x32_bf16(Bt[n][k], At[m][k], acc[ai][bj][m][n], 0, 0, 0); __builtin_amdgcn_s_setprio(0); } while (0)
; #define PG8_WAIT_V(n) asm volatile("s_waitcnt vmcnt(" #n ")" ::: "memory")
; #define PG8_WAIT_L(n) asm volatile("s_waitcnt lgkmcnt(" #n ")" ::: "memory")
; #define PG8_BAR __builtin_amdgcn_s_barrier()
; #define PG8_SCHED __builtin_amdgcn_sched_barrier(0)
; #define PG8_STAGE(bufoff, gbase, voff) do { _Pragma("unroll") for (int _i = 0; _i < 2; ++_i) \
;         __builtin_amdgcn_global_load_lds((const unsigned*)((const char*)(gbase) + (voff)[_i]), (PG8_LAS unsigned*)(lds + (bufoff) + ldsw + _i * 8192), 16, 0, 0); } while (0)
; #define PG8_BAR __builtin_amdgcn_s_barrier()
; template <class Epi, class Sched, bool ALIGN_EPI = false, bool SP2 = false>
; __device__ __forceinline__ void gemm_phase(PG8_LAS unsigned char* lds, const Gemm g, const Sched& S, const Epi& E) {
;     ...
;             PG8_LDB(B0, 0, 0); PG8_LDB(B1, 0, 1); PG8_SCHED; PG8_LDA(At, 0, 0); PG8_STAGE(PG8_SA(1, 1), a1 + hstep, voffA);
;             PG8_WAIT_V(8); PG8_WAIT_L(0); PG8_BAR; PG8_MMA(0, 0, At, B0); PG8_MMA(0, 1, At, B1); PG8_BAR; PG8_SCHED;
;             PG8_LDA(At, 0, 1); PG8_STAGE(PG8_SB(0, 0), b2, voffB); PG8_STAGE(PG8_SB(0, 1), b2 + hstep, voffB); PG8_STAGE(PG8_SA(0, 0), a2, voffA);
;             PG8_WAIT_V(8); PG8_WAIT_L(0); PG8_BAR; PG8_MMA(1, 0, At, B0); PG8_MMA(1, 1, At, B1); PG8_BAR; PG8_SCHED;
.LBB0_332:
	ds_read_b128 v[132:135], v213
	ds_read_b128 v[136:139], v213 offset:1024
	ds_read_b128 v[140:143], v213 offset:2048
	ds_read_b128 v[144:147], v213 offset:3072
	ds_read_b128 v[148:151], v214
	ds_read_b128 v[152:155], v214 offset:1024
	ds_read_b128 v[156:159], v214 offset:2048
	ds_read_b128 v[178:181], v214 offset:3072
	s_add_u32 s2, s0, 0xfff80080
	s_addc_u32 s3, s1, -1
	s_cmp_eq_u32 s95, 28
	s_cselect_b32 s5, s7, s3
	s_cselect_b32 s4, s33, s2
	s_cselect_b32 s3, s53, s85
	s_cselect_b32 s2, s55, s84
	v_lshl_add_u64 v[160:161], s[0:1], 0, v[172:173]
	s_add_i32 m0, s63, 0xc000
	ds_read_b128 v[182:185], v215
	ds_read_b128 v[188:191], v215 offset:1024
	ds_read_b128 v[192:195], v215 offset:2048
	ds_read_b128 v[196:199], v215 offset:3072
	ds_read_b128 v[200:203], v215 offset:4096
	ds_read_b128 v[204:207], v215 offset:5120
	ds_read_b128 v[218:221], v215 offset:6144
	ds_read_b128 v[222:225], v215 offset:7168
	global_load_lds_dwordx4 v[160:161], off
	v_lshl_add_u64 v[160:161], s[0:1], 0, v[174:175]
	s_add_i32 m0, s63, 0xe000
	s_nop 0
	global_load_lds_dwordx4 v[160:161], off
	s_waitcnt vmcnt(8)
	s_waitcnt lgkmcnt(0)
	s_barrier
	s_setprio 1
	s_waitcnt lgkmcnt(0)
	v_mfma_f32_16x16x32_bf16 v[126:129], v[132:135], v[182:185], v[126:129]
	v_mfma_f32_16x16x32_bf16 v[122:125], v[140:143], v[182:185], v[122:125]
	v_mfma_f32_16x16x32_bf16 v[118:121], v[132:135], v[192:195], v[118:121]
	v_mfma_f32_16x16x32_bf16 v[110:113], v[140:143], v[192:195], v[110:113]
	v_mfma_f32_16x16x32_bf16 v[102:105], v[132:135], v[200:203], v[102:105]
	v_mfma_f32_16x16x32_bf16 v[94:97], v[140:143], v[200:203], v[94:97]
	v_mfma_f32_16x16x32_bf16 v[86:89], v[132:135], v[218:221], v[86:89]
	v_mfma_f32_16x16x32_bf16 v[78:81], v[140:143], v[218:221], v[78:81]
	v_mfma_f32_16x16x32_bf16 v[126:129], v[136:139], v[188:191], v[126:129]
	v_mfma_f32_16x16x32_bf16 v[122:125], v[144:147], v[188:191], v[122:125]
	v_mfma_f32_16x16x32_bf16 v[118:121], v[136:139], v[196:199], v[118:121]
	v_mfma_f32_16x16x32_bf16 v[110:113], v[144:147], v[196:199], v[110:113]
	v_mfma_f32_16x16x32_bf16 v[102:105], v[136:139], v[204:207], v[102:105]
	v_mfma_f32_16x16x32_bf16 v[94:97], v[144:147], v[204:207], v[94:97]
	v_mfma_f32_16x16x32_bf16 v[86:89], v[136:139], v[222:225], v[86:89]
	v_mfma_f32_16x16x32_bf16 v[78:81], v[144:147], v[222:225], v[78:81]
	s_setprio 0
	s_setprio 1
	v_mfma_f32_16x16x32_bf16 v[114:117], v[148:151], v[182:185], v[114:117]
	v_mfma_f32_16x16x32_bf16 v[106:109], v[156:159], v[182:185], v[106:109]
	v_mfma_f32_16x16x32_bf16 v[98:101], v[148:151], v[192:195], v[98:101]
	v_mfma_f32_16x16x32_bf16 v[90:93], v[156:159], v[192:195], v[90:93]
	v_mfma_f32_16x16x32_bf16 v[82:85], v[148:151], v[200:203], v[82:85]
	v_mfma_f32_16x16x32_bf16 v[74:77], v[156:159], v[200:203], v[74:77]
	v_mfma_f32_16x16x32_bf16 v[70:73], v[148:151], v[218:221], v[70:73]
	v_mfma_f32_16x16x32_bf16 v[66:69], v[156:159], v[218:221], v[66:69]
	v_mfma_f32_16x16x32_bf16 v[114:117], v[152:155], v[188:191], v[114:117]
	v_mfma_f32_16x16x32_bf16 v[106:109], v[178:181], v[188:191], v[106:109]
	v_mfma_f32_16x16x32_bf16 v[98:101], v[152:155], v[196:199], v[98:101]
	v_mfma_f32_16x16x32_bf16 v[90:93], v[178:181], v[196:199], v[90:93]
	v_mfma_f32_16x16x32_bf16 v[82:85], v[152:155], v[204:207], v[82:85]
	v_mfma_f32_16x16x32_bf16 v[74:77], v[178:181], v[204:207], v[74:77]
	v_mfma_f32_16x16x32_bf16 v[70:73], v[152:155], v[222:225], v[70:73]
	v_mfma_f32_16x16x32_bf16 v[66:69], v[178:181], v[222:225], v[66:69]
	s_setprio 0
	s_barrier
	s_add_i32 s96, s81, s66
	v_lshl_add_u64 v[160:161], s[2:3], 0, v[164:165]
	s_mov_b32 m0, s96
	ds_read_b128 v[182:185], v215 offset:16384
	ds_read_b128 v[188:191], v215 offset:17408
	ds_read_b128 v[192:195], v215 offset:18432
	ds_read_b128 v[196:199], v215 offset:19456
	ds_read_b128 v[200:203], v215 offset:20480
	ds_read_b128 v[204:207], v215 offset:21504
	ds_read_b128 v[218:221], v215 offset:22528
	ds_read_b128 v[222:225], v215 offset:23552
	global_load_lds_dwordx4 v[160:161], off
	s_add_i32 m0, s96, 0x2000
	s_add_u32 s96, s2, 0x80000
	v_lshl_add_u64 v[208:209], s[2:3], 0, v[168:169]
	s_addc_u32 s97, s3, 0
	s_add_i32 vcc_lo, s82, s66
	global_load_lds_dwordx4 v[208:209], off
	v_lshl_add_u64 v[226:227], s[96:97], 0, v[164:165]
	s_mov_b32 m0, vcc_lo
	v_lshl_add_u64 v[228:229], s[4:5], 0, v[166:167]
	global_load_lds_dwordx4 v[226:227], off
	v_lshl_add_u64 v[226:227], s[96:97], 0, v[168:169]
	s_add_i32 m0, vcc_lo, 0x2000
	s_nop 0
	global_load_lds_dwordx4 v[226:227], off
	v_lshl_add_u64 v[226:227], s[4:5], 0, v[162:163]
	s_mov_b32 m0, s63
	s_nop 0
	global_load_lds_dwordx4 v[226:227], off
	s_mov_b32 m0, s65
	s_nop 0
	global_load_lds_dwordx4 v[228:229], off
	s_waitcnt vmcnt(8)
	s_waitcnt lgkmcnt(0)
	s_barrier
; #define PG8_STAGE(bufoff, gbase, voff) do { _Pragma("unroll") for (int _i = 0; _i < 2; ++_i) \
;         __builtin_amdgcn_global_load_lds((const unsigned*)((const char*)(gbase) + (voff)[_i]), (PG8_LAS unsigned*)(lds + (bufoff) + ldsw + _i * 8192), 16, 0, 0); } while (0)
; #define PG8_LDA(dst, b, h) do { _Pragma("unroll") for (int m = 0; m < 4; ++m) _Pragma("unroll") for (int k = 0; k < 2; ++k) dst[m][k] = *(const PG8_LAS bf16x8*)(lds + PG8_SA(b, h) + aoff + m * 2048 + k * 1024); } while (0)
; #define PG8_LDB(dst, b, h) do { _Pragma("unroll") for (int n = 0; n < 2; ++n) _Pragma("unroll") for (int k = 0; k < 2; ++k) dst[n][k] = *(const PG8_LAS bf16x8*)(lds + PG8_SB(b, h) + boff + n * 2048 + k * 1024); } while (0)
; #define PG8_MMA(ai, bj, At, Bt) do { __builtin_amdgcn_s_setprio(1); _Pragma("unroll") for (int m = 0; m < 4; ++m) _Pragma("unroll") for (int n = 0; n < 2; ++n) _Pragma("unroll") for (int k = 0; k < 2; ++k) \
;         acc[ai][bj][m][n] = __builtin_amdgcn_mfma_f32_16x16x32_bf16(Bt[n][k], At[m][k], acc[ai][bj][m][n], 0, 0, 0); __builtin_amdgcn_s_setprio(0); } while (0)
; #define PG8_WAIT_V(n) asm volatile("s_waitcnt vmcnt(" #n ")" ::: "memory")
; #define PG8_WAIT_L(n) asm volatile("s_waitcnt lgkmcnt(" #n ")" ::: "memory")
; #define PG8_BAR __builtin_amdgcn_s_barrier()
; #define PG8_SCHED __builtin_amdgcn_sched_barrier(0)
; #define PG8_STAGE(bufoff, gbase, voff) do { _Pragma("unroll") for (int _i = 0; _i < 2; ++_i) \
;         __builtin_amdgcn_global_load_lds((const unsigned*)((const char*)(gbase) + (voff)[_i]), (PG8_LAS unsigned*)(lds + (bufoff) + ldsw + _i * 8192), 16, 0, 0); } while (0)
; #define PG8_WAIT_V(n) asm volatile("s_waitcnt vmcnt(" #n ")" ::: "memory")
; #define PG8_WAIT_L(n) asm volatile("s_waitcnt lgkmcnt(" #n ")" ::: "memory")
; #define PG8_BAR __builtin_amdgcn_s_barrier()
; template <class Epi, class Sched, bool ALIGN_EPI = false, bool SP2 = false>
; __device__ __forceinline__ void gemm_phase(PG8_LAS unsigned char* lds, const Gemm g, const Sched& S, const Epi& E) {
;     ...
;             PG8_WAIT_V(8); PG8_WAIT_L(0); PG8_BAR; PG8_MMA(1, 0, At, B0); PG8_MMA(1, 1, At, B1); PG8_BAR; PG8_SCHED;
;             PG8_LDB(B0, 1, 0); PG8_LDB(B1, 1, 1); PG8_SCHED; PG8_LDA(At, 1, 0); PG8_STAGE(PG8_SA(0, 1), a2 + hstep, voffA);
;             PG8_WAIT_V(8); PG8_WAIT_L(0); PG8_BAR; PG8_MMA(0, 0, At, B0); PG8_MMA(0, 1, At, B1); PG8_BAR; PG8_SCHED;
	s_setprio 1
	s_waitcnt lgkmcnt(0)
	v_mfma_f32_16x16x32_bf16 v[62:65], v[132:135], v[182:185], v[62:65]
	v_mfma_f32_16x16x32_bf16 v[58:61], v[140:143], v[182:185], v[58:61]
	v_mfma_f32_16x16x32_bf16 v[54:57], v[132:135], v[192:195], v[54:57]
	v_mfma_f32_16x16x32_bf16 v[46:49], v[140:143], v[192:195], v[46:49]
	v_mfma_f32_16x16x32_bf16 v[38:41], v[132:135], v[200:203], v[38:41]
	v_mfma_f32_16x16x32_bf16 v[30:33], v[140:143], v[200:203], v[30:33]
	v_mfma_f32_16x16x32_bf16 v[22:25], v[132:135], v[218:221], v[22:25]
	v_mfma_f32_16x16x32_bf16 v[14:17], v[140:143], v[218:221], v[14:17]
	v_mfma_f32_16x16x32_bf16 v[62:65], v[136:139], v[188:191], v[62:65]
	v_mfma_f32_16x16x32_bf16 v[58:61], v[144:147], v[188:191], v[58:61]
	v_mfma_f32_16x16x32_bf16 v[54:57], v[136:139], v[196:199], v[54:57]
	v_mfma_f32_16x16x32_bf16 v[46:49], v[144:147], v[196:199], v[46:49]
	v_mfma_f32_16x16x32_bf16 v[38:41], v[136:139], v[204:207], v[38:41]
	v_mfma_f32_16x16x32_bf16 v[30:33], v[144:147], v[204:207], v[30:33]
	v_mfma_f32_16x16x32_bf16 v[22:25], v[136:139], v[222:225], v[22:25]
	v_mfma_f32_16x16x32_bf16 v[14:17], v[144:147], v[222:225], v[14:17]
	s_setprio 0
	s_setprio 1
	v_mfma_f32_16x16x32_bf16 v[50:53], v[148:151], v[182:185], v[50:53]
	v_mfma_f32_16x16x32_bf16 v[42:45], v[156:159], v[182:185], v[42:45]
	v_mfma_f32_16x16x32_bf16 v[34:37], v[148:151], v[192:195], v[34:37]
	v_mfma_f32_16x16x32_bf16 v[26:29], v[156:159], v[192:195], v[26:29]
	v_mfma_f32_16x16x32_bf16 v[18:21], v[148:151], v[200:203], v[18:21]
	v_mfma_f32_16x16x32_bf16 v[10:13], v[156:159], v[200:203], v[10:13]
	v_mfma_f32_16x16x32_bf16 v[6:9], v[148:151], v[218:221], v[6:9]
	v_mfma_f32_16x16x32_bf16 v[2:5], v[156:159], v[218:221], v[2:5]
	v_mfma_f32_16x16x32_bf16 v[50:53], v[152:155], v[188:191], v[50:53]
	v_mfma_f32_16x16x32_bf16 v[42:45], v[178:181], v[188:191], v[42:45]
	v_mfma_f32_16x16x32_bf16 v[34:37], v[152:155], v[196:199], v[34:37]
	v_mfma_f32_16x16x32_bf16 v[26:29], v[178:181], v[196:199], v[26:29]
	v_mfma_f32_16x16x32_bf16 v[18:21], v[152:155], v[204:207], v[18:21]
	v_mfma_f32_16x16x32_bf16 v[10:13], v[178:181], v[204:207], v[10:13]
	v_mfma_f32_16x16x32_bf16 v[6:9], v[152:155], v[222:225], v[6:9]
	v_mfma_f32_16x16x32_bf16 v[2:5], v[178:181], v[222:225], v[2:5]
	s_setprio 0
	s_barrier
	s_add_i32 s96, 0, 0x18000
	v_add_u32_e32 v131, s96, v211
	s_add_i32 s97, 0, 0x1c000
	ds_read_b128 v[132:135], v131
	ds_read_b128 v[136:139], v131 offset:1024
	ds_read_b128 v[140:143], v131 offset:2048
	ds_read_b128 v[144:147], v131 offset:3072
	v_add_u32_e32 v131, s97, v211
	ds_read_b128 v[148:151], v131
	ds_read_b128 v[152:155], v131 offset:1024
	ds_read_b128 v[156:159], v131 offset:2048
	ds_read_b128 v[178:181], v131 offset:3072
	s_add_u32 s4, s4, 0x80000
	s_addc_u32 s5, s5, 0
	s_mov_b32 m0, s71
	v_lshl_add_u64 v[230:231], s[4:5], 0, v[162:163]
	ds_read_b128 v[182:185], v215 offset:32768
	ds_read_b128 v[188:191], v215 offset:33792
	ds_read_b128 v[192:195], v215 offset:34816
	ds_read_b128 v[196:199], v215 offset:35840
	ds_read_b128 v[200:203], v215 offset:36864
	ds_read_b128 v[204:207], v215 offset:37888
	ds_read_b128 v[218:221], v215 offset:38912
	ds_read_b128 v[222:225], v215 offset:39936
	global_load_lds_dwordx4 v[230:231], off
	v_lshl_add_u64 v[230:231], s[4:5], 0, v[166:167]
	s_mov_b32 m0, s72
	s_nop 0
	global_load_lds_dwordx4 v[230:231], off
	s_waitcnt vmcnt(8)
	s_waitcnt lgkmcnt(0)
	s_barrier
	s_setprio 1
	s_waitcnt lgkmcnt(0)
	v_mfma_f32_16x16x32_bf16 v[126:129], v[132:135], v[182:185], v[126:129]
	v_mfma_f32_16x16x32_bf16 v[122:125], v[140:143], v[182:185], v[122:125]
	v_mfma_f32_16x16x32_bf16 v[118:121], v[132:135], v[192:195], v[118:121]
	v_mfma_f32_16x16x32_bf16 v[110:113], v[140:143], v[192:195], v[110:113]
	v_mfma_f32_16x16x32_bf16 v[102:105], v[132:135], v[200:203], v[102:105]
	v_mfma_f32_16x16x32_bf16 v[94:97], v[140:143], v[200:203], v[94:97]
	v_mfma_f32_16x16x32_bf16 v[86:89], v[132:135], v[218:221], v[86:89]
	v_mfma_f32_16x16x32_bf16 v[78:81], v[140:143], v[218:221], v[78:81]
	v_mfma_f32_16x16x32_bf16 v[126:129], v[136:139], v[188:191], v[126:129]
	v_mfma_f32_16x16x32_bf16 v[122:125], v[144:147], v[188:191], v[122:125]
	v_mfma_f32_16x16x32_bf16 v[118:121], v[136:139], v[196:199], v[118:121]
	v_mfma_f32_16x16x32_bf16 v[110:113], v[144:147], v[196:199], v[110:113]
	v_mfma_f32_16x16x32_bf16 v[102:105], v[136:139], v[204:207], v[102:105]
	v_mfma_f32_16x16x32_bf16 v[94:97], v[144:147], v[204:207], v[94:97]
	v_mfma_f32_16x16x32_bf16 v[86:89], v[136:139], v[222:225], v[86:89]
	v_mfma_f32_16x16x32_bf16 v[78:81], v[144:147], v[222:225], v[78:81]
	s_setprio 0
	s_setprio 1
	v_mfma_f32_16x16x32_bf16 v[114:117], v[148:151], v[182:185], v[114:117]
	v_mfma_f32_16x16x32_bf16 v[106:109], v[156:159], v[182:185], v[106:109]
	v_mfma_f32_16x16x32_bf16 v[98:101], v[148:151], v[192:195], v[98:101]
	v_mfma_f32_16x16x32_bf16 v[90:93], v[156:159], v[192:195], v[90:93]
	v_mfma_f32_16x16x32_bf16 v[82:85], v[148:151], v[200:203], v[82:85]
	v_mfma_f32_16x16x32_bf16 v[74:77], v[156:159], v[200:203], v[74:77]
	v_mfma_f32_16x16x32_bf16 v[70:73], v[148:151], v[218:221], v[70:73]
	v_mfma_f32_16x16x32_bf16 v[66:69], v[156:159], v[218:221], v[66:69]
	v_mfma_f32_16x16x32_bf16 v[114:117], v[152:155], v[188:191], v[114:117]
	v_mfma_f32_16x16x32_bf16 v[106:109], v[178:181], v[188:191], v[106:109]
	v_mfma_f32_16x16x32_bf16 v[98:101], v[152:155], v[196:199], v[98:101]
	v_mfma_f32_16x16x32_bf16 v[90:93], v[178:181], v[196:199], v[90:93]
	v_mfma_f32_16x16x32_bf16 v[82:85], v[152:155], v[204:207], v[82:85]
	v_mfma_f32_16x16x32_bf16 v[74:77], v[178:181], v[204:207], v[74:77]
	v_mfma_f32_16x16x32_bf16 v[70:73], v[152:155], v[222:225], v[70:73]
	v_mfma_f32_16x16x32_bf16 v[66:69], v[178:181], v[222:225], v[66:69]
	s_setprio 0
	s_barrier
; #define PG8_STAGE(bufoff, gbase, voff) do { _Pragma("unroll") for (int _i = 0; _i < 2; ++_i) \
;         __builtin_amdgcn_global_load_lds((const unsigned*)((const char*)(gbase) + (voff)[_i]), (PG8_LAS unsigned*)(lds + (bufoff) + ldsw + _i * 8192), 16, 0, 0); } while (0)
; #define PG8_LDA(dst, b, h) do { _Pragma("unroll") for (int m = 0; m < 4; ++m) _Pragma("unroll") for (int k = 0; k < 2; ++k) dst[m][k] = *(const PG8_LAS bf16x8*)(lds + PG8_SA(b, h) + aoff + m * 2048 + k * 1024); } while (0)
; #define PG8_MMA(ai, bj, At, Bt) do { __builtin_amdgcn_s_setprio(1); _Pragma("unroll") for (int m = 0; m < 4; ++m) _Pragma("unroll") for (int n = 0; n < 2; ++n) _Pragma("unroll") for (int k = 0; k < 2; ++k) \
;         acc[ai][bj][m][n] = __builtin_amdgcn_mfma_f32_16x16x32_bf16(Bt[n][k], At[m][k], acc[ai][bj][m][n], 0, 0, 0); __builtin_amdgcn_s_setprio(0); } while (0)
; #define PG8_WAIT_V(n) asm volatile("s_waitcnt vmcnt(" #n ")" ::: "memory")
; #define PG8_WAIT_L(n) asm volatile("s_waitcnt lgkmcnt(" #n ")" ::: "memory")
; #define PG8_BAR __builtin_amdgcn_s_barrier()
; #define PG8_SCHED __builtin_amdgcn_sched_barrier(0)
; #define PG8_STAGE(bufoff, gbase, voff) do { _Pragma("unroll") for (int _i = 0; _i < 2; ++_i) \
;         __builtin_amdgcn_global_load_lds((const unsigned*)((const char*)(gbase) + (voff)[_i]), (PG8_LAS unsigned*)(lds + (bufoff) + ldsw + _i * 8192), 16, 0, 0); } while (0)
; #define PG8_LDA(dst, b, h) do { _Pragma("unroll") for (int m = 0; m < 4; ++m) _Pragma("unroll") for (int k = 0; k < 2; ++k) dst[m][k] = *(const PG8_LAS bf16x8*)(lds + PG8_SA(b, h) + aoff + m * 2048 + k * 1024); } while (0)
; #define PG8_WAIT_V(n) asm volatile("s_waitcnt vmcnt(" #n ")" ::: "memory")
; #define PG8_WAIT_L(n) asm volatile("s_waitcnt lgkmcnt(" #n ")" ::: "memory")
; #define PG8_BAR __builtin_amdgcn_s_barrier()
; #define PG8_SCHED __builtin_amdgcn_sched_barrier(0)
; template <class Epi, class Sched, bool ALIGN_EPI = false, bool SP2 = false>
; __device__ __forceinline__ void gemm_phase(PG8_LAS unsigned char* lds, const Gemm g, const Sched& S, const Epi& E) {
;     ...
;             PG8_LDA(At, 1, 1); PG8_STAGE(PG8_SB(1, 0), b3, voffB); PG8_STAGE(PG8_SB(1, 1), b3 + hstep, voffB); PG8_STAGE(PG8_SA(1, 0), a3, voffA);
;             PG8_WAIT_V(8); PG8_WAIT_L(0); PG8_BAR; PG8_MMA(1, 0, At, B0); PG8_MMA(1, 1, At, B1); PG8_BAR; PG8_SCHED;
	s_add_i32 s4, s96, s66
	v_lshl_add_u64 v[160:161], v[160:161], 0, s[40:41]
	s_mov_b32 m0, s4
	ds_read_b128 v[182:185], v215 offset:49152
	ds_read_b128 v[188:191], v215 offset:50176
	ds_read_b128 v[192:195], v215 offset:51200
	ds_read_b128 v[196:199], v215 offset:52224
	ds_read_b128 v[200:203], v215 offset:53248
	ds_read_b128 v[204:207], v215 offset:54272
	ds_read_b128 v[218:221], v215 offset:55296
	ds_read_b128 v[222:225], v215 offset:56320
	global_load_lds_dwordx4 v[160:161], off
	s_add_i32 m0, s4, 0x2000
	s_add_u32 s2, s2, 0x80080
	v_lshl_add_u64 v[160:161], v[208:209], 0, s[40:41]
	s_addc_u32 s3, s3, 0
	s_add_i32 s4, s97, s66
	global_load_lds_dwordx4 v[160:161], off
	v_lshl_add_u64 v[160:161], s[2:3], 0, v[164:165]
	s_mov_b32 m0, s4
	s_nop 0
	global_load_lds_dwordx4 v[160:161], off
	v_lshl_add_u64 v[160:161], s[2:3], 0, v[168:169]
	s_add_i32 m0, s4, 0x2000
	s_nop 0
	global_load_lds_dwordx4 v[160:161], off
	v_lshl_add_u64 v[160:161], v[226:227], 0, s[40:41]
	s_mov_b32 m0, s74
	s_nop 0
	global_load_lds_dwordx4 v[160:161], off
	v_lshl_add_u64 v[160:161], v[228:229], 0, s[40:41]
	s_mov_b32 m0, s75
	s_nop 0
	global_load_lds_dwordx4 v[160:161], off
	s_waitcnt vmcnt(8)
	s_waitcnt lgkmcnt(0)
	s_barrier
	s_setprio 1
	s_waitcnt lgkmcnt(0)
	v_mfma_f32_16x16x32_bf16 v[62:65], v[132:135], v[182:185], v[62:65]
	v_mfma_f32_16x16x32_bf16 v[58:61], v[140:143], v[182:185], v[58:61]
	v_mfma_f32_16x16x32_bf16 v[54:57], v[132:135], v[192:195], v[54:57]
	v_mfma_f32_16x16x32_bf16 v[46:49], v[140:143], v[192:195], v[46:49]
	v_mfma_f32_16x16x32_bf16 v[38:41], v[132:135], v[200:203], v[38:41]
	v_mfma_f32_16x16x32_bf16 v[30:33], v[140:143], v[200:203], v[30:33]
	v_mfma_f32_16x16x32_bf16 v[22:25], v[132:135], v[218:221], v[22:25]
	v_mfma_f32_16x16x32_bf16 v[14:17], v[140:143], v[218:221], v[14:17]
	v_mfma_f32_16x16x32_bf16 v[62:65], v[136:139], v[188:191], v[62:65]
	v_mfma_f32_16x16x32_bf16 v[58:61], v[144:147], v[188:191], v[58:61]
	v_mfma_f32_16x16x32_bf16 v[54:57], v[136:139], v[196:199], v[54:57]
	v_mfma_f32_16x16x32_bf16 v[46:49], v[144:147], v[196:199], v[46:49]
	v_mfma_f32_16x16x32_bf16 v[38:41], v[136:139], v[204:207], v[38:41]
	v_mfma_f32_16x16x32_bf16 v[30:33], v[144:147], v[204:207], v[30:33]
	v_mfma_f32_16x16x32_bf16 v[22:25], v[136:139], v[222:225], v[22:25]
	v_mfma_f32_16x16x32_bf16 v[14:17], v[144:147], v[222:225], v[14:17]
	s_setprio 0
	s_setprio 1
	v_mfma_f32_16x16x32_bf16 v[50:53], v[148:151], v[182:185], v[50:53]
	v_mfma_f32_16x16x32_bf16 v[42:45], v[156:159], v[182:185], v[42:45]
	v_mfma_f32_16x16x32_bf16 v[34:37], v[148:151], v[192:195], v[34:37]
	v_mfma_f32_16x16x32_bf16 v[26:29], v[156:159], v[192:195], v[26:29]
	v_mfma_f32_16x16x32_bf16 v[18:21], v[148:151], v[200:203], v[18:21]
	v_mfma_f32_16x16x32_bf16 v[10:13], v[156:159], v[200:203], v[10:13]
	v_mfma_f32_16x16x32_bf16 v[6:9], v[148:151], v[218:221], v[6:9]
	v_mfma_f32_16x16x32_bf16 v[2:5], v[156:159], v[218:221], v[2:5]
	v_mfma_f32_16x16x32_bf16 v[50:53], v[152:155], v[188:191], v[50:53]
	v_mfma_f32_16x16x32_bf16 v[42:45], v[178:181], v[188:191], v[42:45]
	v_mfma_f32_16x16x32_bf16 v[34:37], v[152:155], v[196:199], v[34:37]
	v_mfma_f32_16x16x32_bf16 v[26:29], v[178:181], v[196:199], v[26:29]
	v_mfma_f32_16x16x32_bf16 v[18:21], v[152:155], v[204:207], v[18:21]
	v_mfma_f32_16x16x32_bf16 v[10:13], v[178:181], v[204:207], v[10:13]
	v_mfma_f32_16x16x32_bf16 v[6:9], v[152:155], v[222:225], v[6:9]
	v_mfma_f32_16x16x32_bf16 v[2:5], v[178:181], v[222:225], v[2:5]
	s_setprio 0
	s_barrier
	s_add_i32 s95, s95, 2
	s_add_u32 s0, s0, 0x100
	s_addc_u32 s1, s1, 0
	s_add_u32 s84, s84, 0x100
	s_addc_u32 s85, s85, 0
	s_cmp_gt_u32 s95, 29
	s_cbranch_scc0 .LBB0_332
	s_waitcnt vmcnt(8)
	v_readfirstlane_b32 s2, v130
	s_and_saveexec_b64 s[0:1], s[10:11]
	s_cbranch_execz .LBB0_335
	s_and_b32 s3, s6, 3
	s_xor_b32 s3, s3, 2
	s_and_b64 s[4:5], s[42:43], exec
	s_cselect_b32 s3, s3, s76
	s_lshl_b32 s3, s3, 2
	s_add_i32 s3, s3, 0
	s_add_i32 s3, s3, 0x27da0
	v_mov_b32_e32 v130, s3
	v_mov_b32_e32 v131, s2
	ds_write_b32 v130, v131
